# hyconv latent epilogue: w/x0 row batches loaded two at a time (2 memory round trips per unit instead of 4), second batch on renamed registers
# speedup vs baseline: 1.0067x; 1.0009x over previous
.LBB0_822:
	v_lshl_add_u64 v[2:3], v[26:27], 0, s[2:3]
	v_add_co_u32_e32 v4, vcc, 0x32600000, v2
	s_nop 1
	v_addc_co_u32_e32 v5, vcc, 0, v3, vcc
	v_add_co_u32_e32 v48, vcc, 0x41600000, v2
	s_nop 1
	v_addc_co_u32_e32 v49, vcc, 0, v3, vcc
	global_load_dwordx4 v[36:39], v[4:5], off
	global_load_dwordx4 v[40:43], v[48:49], off
	v_add_co_u32_e32 v4, vcc, 0x32602000, v2
	s_nop 1
	v_addc_co_u32_e32 v5, vcc, 0, v3, vcc
	v_add_co_u32_e32 v32, vcc, 0x41602000, v2
	s_nop 1
	v_addc_co_u32_e32 v33, vcc, 0, v3, vcc
	global_load_dwordx4 v[18:21], v[4:5], off offset:256
	global_load_dwordx4 v[22:25], v[32:33], off offset:256
	v_add_co_u32_e32 v4, vcc, 0x32604000, v2
	s_nop 1
	v_addc_co_u32_e32 v5, vcc, 0, v3, vcc
	v_add_co_u32_e32 v30, vcc, 0x41604000, v2
	s_nop 1
	v_addc_co_u32_e32 v31, vcc, 0, v3, vcc
	global_load_dwordx4 v[10:13], v[4:5], off offset:512
	global_load_dwordx4 v[14:17], v[30:31], off offset:512
	v_add_co_u32_e32 v4, vcc, 0x32606000, v2
	s_nop 1
	v_addc_co_u32_e32 v5, vcc, 0, v3, vcc
	v_add_co_u32_e32 v28, vcc, 0x41606000, v2
	s_nop 1
	v_addc_co_u32_e32 v29, vcc, 0, v3, vcc
	global_load_dwordx4 v[2:5], v[4:5], off offset:768
	s_nop 0
	global_load_dwordx4 v[6:9], v[28:29], off offset:768
	s_add_u32 s2, s2, 0x8400
	s_addc_u32 s3, s3, 0
	v_lshl_add_u64 v[76:77], v[26:27], 0, s[2:3]
	v_add_co_u32_e32 v78, vcc, 0x32600000, v76
	s_nop 1
	v_addc_co_u32_e32 v79, vcc, 0, v77, vcc
	v_add_co_u32_e32 v122, vcc, 0x41600000, v76
	s_nop 1
	v_addc_co_u32_e32 v123, vcc, 0, v77, vcc
	global_load_dwordx4 v[110:113], v[78:79], off
	global_load_dwordx4 v[114:117], v[122:123], off
	v_add_co_u32_e32 v78, vcc, 0x32602000, v76
	s_nop 1
	v_addc_co_u32_e32 v79, vcc, 0, v77, vcc
	v_add_co_u32_e32 v106, vcc, 0x41602000, v76
	s_nop 1
	v_addc_co_u32_e32 v107, vcc, 0, v77, vcc
	global_load_dwordx4 v[92:95], v[78:79], off offset:256
	global_load_dwordx4 v[96:99], v[106:107], off offset:256
	v_add_co_u32_e32 v78, vcc, 0x32604000, v76
	s_nop 1
	v_addc_co_u32_e32 v79, vcc, 0, v77, vcc
	v_add_co_u32_e32 v104, vcc, 0x41604000, v76
	s_nop 1
	v_addc_co_u32_e32 v105, vcc, 0, v77, vcc
	global_load_dwordx4 v[84:87], v[78:79], off offset:512
	global_load_dwordx4 v[88:91], v[104:105], off offset:512
	v_add_co_u32_e32 v78, vcc, 0x32606000, v76
	s_nop 1
	v_addc_co_u32_e32 v79, vcc, 0, v77, vcc
	v_add_co_u32_e32 v102, vcc, 0x41606000, v76
	s_nop 1
	v_addc_co_u32_e32 v103, vcc, 0, v77, vcc
	global_load_dwordx4 v[76:79], v[78:79], off offset:768
	s_nop 0
	global_load_dwordx4 v[80:83], v[102:103], off offset:768
	ds_read_b128 v[44:47], v1
	s_waitcnt vmcnt(15)
	v_lshlrev_b32_e32 v54, 16, v36
	v_and_b32_e32 v55, 0xffff0000, v36
	s_waitcnt vmcnt(14)
	v_lshlrev_b32_e32 v50, 16, v40
	v_and_b32_e32 v51, 0xffff0000, v40
	s_waitcnt lgkmcnt(0)
	v_lshlrev_b32_e32 v52, 16, v44
	v_and_b32_e32 v53, 0xffff0000, v44
	v_pk_fma_f32 v[52:53], v[132:133], v[54:55], v[52:53]
	v_lshlrev_b32_e32 v44, 16, v45
	v_pk_mul_f32 v[50:51], v[52:53], v[50:51]
	v_and_b32_e32 v45, 0xffff0000, v45
	v_cvt_pk_bf16_f32 v36, v50, v51
	v_lshlrev_b32_e32 v50, 16, v37
	v_and_b32_e32 v51, 0xffff0000, v37
	v_lshlrev_b32_e32 v40, 16, v41
	v_and_b32_e32 v41, 0xffff0000, v41
	v_pk_fma_f32 v[44:45], v[132:133], v[50:51], v[44:45]
	v_lshlrev_b32_e32 v50, 16, v38
	v_pk_mul_f32 v[40:41], v[44:45], v[40:41]
	v_lshlrev_b32_e32 v44, 16, v46
	v_and_b32_e32 v45, 0xffff0000, v46
	v_and_b32_e32 v51, 0xffff0000, v38
	v_cvt_pk_bf16_f32 v37, v40, v41
	v_lshlrev_b32_e32 v40, 16, v42
	v_and_b32_e32 v41, 0xffff0000, v42
	v_pk_fma_f32 v[44:45], v[132:133], v[50:51], v[44:45]
	v_lshlrev_b32_e32 v42, 16, v47
	v_pk_mul_f32 v[40:41], v[44:45], v[40:41]
	v_lshlrev_b32_e32 v44, 16, v39
	v_cvt_pk_bf16_f32 v38, v40, v41
	v_lshlrev_b32_e32 v40, 16, v43
	v_and_b32_e32 v41, 0xffff0000, v43
	v_and_b32_e32 v43, 0xffff0000, v47
	v_and_b32_e32 v45, 0xffff0000, v39
	v_pk_fma_f32 v[42:43], v[132:133], v[44:45], v[42:43]
	s_waitcnt vmcnt(13)
	v_lshlrev_b32_e32 v44, 16, v18
	v_pk_mul_f32 v[40:41], v[42:43], v[40:41]
	v_and_b32_e32 v45, 0xffff0000, v18
	v_cvt_pk_bf16_f32 v39, v40, v41
	global_store_dwordx4 v[48:49], v[36:39], off
	ds_read_b128 v[36:39], v1 offset:1056
	s_waitcnt vmcnt(13)
	v_lshlrev_b32_e32 v40, 16, v22
	v_and_b32_e32 v41, 0xffff0000, v22
	v_lshlrev_b32_e32 v22, 16, v23
	v_and_b32_e32 v23, 0xffff0000, v23
	s_waitcnt lgkmcnt(0)
	v_lshlrev_b32_e32 v42, 16, v36
	v_and_b32_e32 v43, 0xffff0000, v36
	v_pk_fma_f32 v[42:43], v[132:133], v[44:45], v[42:43]
	v_lshlrev_b32_e32 v36, 16, v37
	v_pk_mul_f32 v[40:41], v[42:43], v[40:41]
	v_and_b32_e32 v37, 0xffff0000, v37
	v_cvt_pk_bf16_f32 v18, v40, v41
	v_lshlrev_b32_e32 v40, 16, v19
	v_and_b32_e32 v41, 0xffff0000, v19
	v_pk_fma_f32 v[36:37], v[132:133], v[40:41], v[36:37]
	v_lshlrev_b32_e32 v40, 16, v20
	v_pk_mul_f32 v[22:23], v[36:37], v[22:23]
	v_lshlrev_b32_e32 v36, 16, v38
	v_and_b32_e32 v37, 0xffff0000, v38
	v_and_b32_e32 v41, 0xffff0000, v20
	v_cvt_pk_bf16_f32 v19, v22, v23
	v_lshlrev_b32_e32 v22, 16, v24
	v_and_b32_e32 v23, 0xffff0000, v24
	v_pk_fma_f32 v[36:37], v[132:133], v[40:41], v[36:37]
	v_lshlrev_b32_e32 v24, 16, v39
	v_pk_mul_f32 v[22:23], v[36:37], v[22:23]
	v_lshlrev_b32_e32 v36, 16, v21
	v_cvt_pk_bf16_f32 v20, v22, v23
	v_lshlrev_b32_e32 v22, 16, v25
	v_and_b32_e32 v23, 0xffff0000, v25
	v_and_b32_e32 v25, 0xffff0000, v39
	v_and_b32_e32 v37, 0xffff0000, v21
	v_pk_fma_f32 v[24:25], v[132:133], v[36:37], v[24:25]
	s_nop 0
	v_pk_mul_f32 v[22:23], v[24:25], v[22:23]
	s_nop 0
	v_cvt_pk_bf16_f32 v21, v22, v23
	global_store_dwordx4 v[32:33], v[18:21], off offset:256
	ds_read_b128 v[18:21], v1 offset:2112
	s_waitcnt vmcnt(13)
	v_lshlrev_b32_e32 v32, 16, v10
	v_and_b32_e32 v33, 0xffff0000, v10
	s_waitcnt vmcnt(12)
	v_lshlrev_b32_e32 v22, 16, v14
	v_and_b32_e32 v23, 0xffff0000, v14
	s_waitcnt lgkmcnt(0)
	v_lshlrev_b32_e32 v24, 16, v18
	v_and_b32_e32 v25, 0xffff0000, v18
	v_pk_fma_f32 v[24:25], v[132:133], v[32:33], v[24:25]
	v_lshlrev_b32_e32 v18, 16, v19
	v_pk_mul_f32 v[22:23], v[24:25], v[22:23]
	v_and_b32_e32 v19, 0xffff0000, v19
	v_cvt_pk_bf16_f32 v10, v22, v23
	v_lshlrev_b32_e32 v22, 16, v11
	v_and_b32_e32 v23, 0xffff0000, v11
	v_lshlrev_b32_e32 v14, 16, v15
	v_and_b32_e32 v15, 0xffff0000, v15
	v_pk_fma_f32 v[18:19], v[132:133], v[22:23], v[18:19]
	v_lshlrev_b32_e32 v22, 16, v12
	v_pk_mul_f32 v[14:15], v[18:19], v[14:15]
	v_lshlrev_b32_e32 v18, 16, v20
	v_and_b32_e32 v19, 0xffff0000, v20
	v_and_b32_e32 v23, 0xffff0000, v12
	v_cvt_pk_bf16_f32 v11, v14, v15
	v_lshlrev_b32_e32 v14, 16, v16
	v_and_b32_e32 v15, 0xffff0000, v16
	v_pk_fma_f32 v[18:19], v[132:133], v[22:23], v[18:19]
	v_lshlrev_b32_e32 v16, 16, v21
	v_pk_mul_f32 v[14:15], v[18:19], v[14:15]
	v_lshlrev_b32_e32 v18, 16, v13
	v_cvt_pk_bf16_f32 v12, v14, v15
	v_lshlrev_b32_e32 v14, 16, v17
	v_and_b32_e32 v15, 0xffff0000, v17
	v_and_b32_e32 v17, 0xffff0000, v21
	v_and_b32_e32 v19, 0xffff0000, v13
	v_pk_fma_f32 v[16:17], v[132:133], v[18:19], v[16:17]
	s_waitcnt vmcnt(11)
	v_lshlrev_b32_e32 v18, 16, v2
	v_pk_mul_f32 v[14:15], v[16:17], v[14:15]
	v_and_b32_e32 v19, 0xffff0000, v2
	v_cvt_pk_bf16_f32 v13, v14, v15
	global_store_dwordx4 v[30:31], v[10:13], off offset:512
	ds_read_b128 v[10:13], v1 offset:3168
	s_waitcnt vmcnt(11)
	v_lshlrev_b32_e32 v14, 16, v6
	v_and_b32_e32 v15, 0xffff0000, v6
	v_lshlrev_b32_e32 v6, 16, v7
	v_and_b32_e32 v7, 0xffff0000, v7
	s_waitcnt lgkmcnt(0)
	v_lshlrev_b32_e32 v16, 16, v10
	v_and_b32_e32 v17, 0xffff0000, v10
	v_pk_fma_f32 v[16:17], v[132:133], v[18:19], v[16:17]
	v_lshlrev_b32_e32 v10, 16, v11
	v_pk_mul_f32 v[14:15], v[16:17], v[14:15]
	v_and_b32_e32 v11, 0xffff0000, v11
	v_cvt_pk_bf16_f32 v2, v14, v15
	v_lshlrev_b32_e32 v14, 16, v3
	v_and_b32_e32 v15, 0xffff0000, v3
	v_pk_fma_f32 v[10:11], v[132:133], v[14:15], v[10:11]
	v_lshlrev_b32_e32 v14, 16, v4
	v_pk_mul_f32 v[6:7], v[10:11], v[6:7]
	v_lshlrev_b32_e32 v10, 16, v12
	v_and_b32_e32 v11, 0xffff0000, v12
	v_and_b32_e32 v15, 0xffff0000, v4
	v_cvt_pk_bf16_f32 v3, v6, v7
	v_lshlrev_b32_e32 v6, 16, v8
	v_and_b32_e32 v7, 0xffff0000, v8
	v_pk_fma_f32 v[10:11], v[132:133], v[14:15], v[10:11]
	v_lshlrev_b32_e32 v8, 16, v13
	v_pk_mul_f32 v[6:7], v[10:11], v[6:7]
	v_lshlrev_b32_e32 v10, 16, v5
	v_cvt_pk_bf16_f32 v4, v6, v7
	v_lshlrev_b32_e32 v6, 16, v9
	v_and_b32_e32 v7, 0xffff0000, v9
	v_and_b32_e32 v9, 0xffff0000, v13
	v_and_b32_e32 v11, 0xffff0000, v5
	v_pk_fma_f32 v[8:9], v[132:133], v[10:11], v[8:9]
	s_nop 0
	v_pk_mul_f32 v[6:7], v[8:9], v[6:7]
	s_nop 0
	v_cvt_pk_bf16_f32 v5, v6, v7
	global_store_dwordx4 v[28:29], v[2:5], off offset:768
	ds_read_b128 v[118:121], v1 offset:4224
	s_waitcnt vmcnt(11)
	v_lshlrev_b32_e32 v128, 16, v110
	v_and_b32_e32 v129, 0xffff0000, v110
	s_waitcnt vmcnt(10)
	v_lshlrev_b32_e32 v124, 16, v114
	v_and_b32_e32 v125, 0xffff0000, v114
	s_waitcnt lgkmcnt(0)
	v_lshlrev_b32_e32 v126, 16, v118
	v_and_b32_e32 v127, 0xffff0000, v118
	v_pk_fma_f32 v[126:127], v[132:133], v[128:129], v[126:127]
	v_lshlrev_b32_e32 v118, 16, v119
	v_pk_mul_f32 v[124:125], v[126:127], v[124:125]
	v_and_b32_e32 v119, 0xffff0000, v119
	v_cvt_pk_bf16_f32 v110, v124, v125
	v_lshlrev_b32_e32 v124, 16, v111
	v_and_b32_e32 v125, 0xffff0000, v111
	v_lshlrev_b32_e32 v114, 16, v115
	v_and_b32_e32 v115, 0xffff0000, v115
	v_pk_fma_f32 v[118:119], v[132:133], v[124:125], v[118:119]
	v_lshlrev_b32_e32 v124, 16, v112
	v_pk_mul_f32 v[114:115], v[118:119], v[114:115]
	v_lshlrev_b32_e32 v118, 16, v120
	v_and_b32_e32 v119, 0xffff0000, v120
	v_and_b32_e32 v125, 0xffff0000, v112
	v_cvt_pk_bf16_f32 v111, v114, v115
	v_lshlrev_b32_e32 v114, 16, v116
	v_and_b32_e32 v115, 0xffff0000, v116
	v_pk_fma_f32 v[118:119], v[132:133], v[124:125], v[118:119]
	v_lshlrev_b32_e32 v116, 16, v121
	v_pk_mul_f32 v[114:115], v[118:119], v[114:115]
	v_lshlrev_b32_e32 v118, 16, v113
	v_cvt_pk_bf16_f32 v112, v114, v115
	v_lshlrev_b32_e32 v114, 16, v117
	v_and_b32_e32 v115, 0xffff0000, v117
	v_and_b32_e32 v117, 0xffff0000, v121
	v_and_b32_e32 v119, 0xffff0000, v113
	v_pk_fma_f32 v[116:117], v[132:133], v[118:119], v[116:117]
	s_waitcnt vmcnt(9)
	v_lshlrev_b32_e32 v118, 16, v92
	v_pk_mul_f32 v[114:115], v[116:117], v[114:115]
	v_and_b32_e32 v119, 0xffff0000, v92
	v_cvt_pk_bf16_f32 v113, v114, v115
	global_store_dwordx4 v[122:123], v[110:113], off
	ds_read_b128 v[110:113], v1 offset:5280
	s_waitcnt vmcnt(9)
	v_lshlrev_b32_e32 v114, 16, v96
	v_and_b32_e32 v115, 0xffff0000, v96
	v_lshlrev_b32_e32 v96, 16, v97
	v_and_b32_e32 v97, 0xffff0000, v97
	s_waitcnt lgkmcnt(0)
	v_lshlrev_b32_e32 v116, 16, v110
	v_and_b32_e32 v117, 0xffff0000, v110
	v_pk_fma_f32 v[116:117], v[132:133], v[118:119], v[116:117]
	v_lshlrev_b32_e32 v110, 16, v111
	v_pk_mul_f32 v[114:115], v[116:117], v[114:115]
	v_and_b32_e32 v111, 0xffff0000, v111
	v_cvt_pk_bf16_f32 v92, v114, v115
	v_lshlrev_b32_e32 v114, 16, v93
	v_and_b32_e32 v115, 0xffff0000, v93
	v_pk_fma_f32 v[110:111], v[132:133], v[114:115], v[110:111]
	v_lshlrev_b32_e32 v114, 16, v94
	v_pk_mul_f32 v[96:97], v[110:111], v[96:97]
	v_lshlrev_b32_e32 v110, 16, v112
	v_and_b32_e32 v111, 0xffff0000, v112
	v_and_b32_e32 v115, 0xffff0000, v94
	v_cvt_pk_bf16_f32 v93, v96, v97
	v_lshlrev_b32_e32 v96, 16, v98
	v_and_b32_e32 v97, 0xffff0000, v98
	v_pk_fma_f32 v[110:111], v[132:133], v[114:115], v[110:111]
	v_lshlrev_b32_e32 v98, 16, v113
	v_pk_mul_f32 v[96:97], v[110:111], v[96:97]
	v_lshlrev_b32_e32 v110, 16, v95
	v_cvt_pk_bf16_f32 v94, v96, v97
	v_lshlrev_b32_e32 v96, 16, v99
	v_and_b32_e32 v97, 0xffff0000, v99
	v_and_b32_e32 v99, 0xffff0000, v113
	v_and_b32_e32 v111, 0xffff0000, v95
	v_pk_fma_f32 v[98:99], v[132:133], v[110:111], v[98:99]
	s_nop 0
	v_pk_mul_f32 v[96:97], v[98:99], v[96:97]
	s_nop 0
	v_cvt_pk_bf16_f32 v95, v96, v97
	global_store_dwordx4 v[106:107], v[92:95], off offset:256
	ds_read_b128 v[92:95], v1 offset:6336
	s_waitcnt vmcnt(9)
	v_lshlrev_b32_e32 v106, 16, v84
	v_and_b32_e32 v107, 0xffff0000, v84
	s_waitcnt vmcnt(8)
	v_lshlrev_b32_e32 v96, 16, v88
	v_and_b32_e32 v97, 0xffff0000, v88
	s_waitcnt lgkmcnt(0)
	v_lshlrev_b32_e32 v98, 16, v92
	v_and_b32_e32 v99, 0xffff0000, v92
	v_pk_fma_f32 v[98:99], v[132:133], v[106:107], v[98:99]
	v_lshlrev_b32_e32 v92, 16, v93
	v_pk_mul_f32 v[96:97], v[98:99], v[96:97]
	v_and_b32_e32 v93, 0xffff0000, v93
	v_cvt_pk_bf16_f32 v84, v96, v97
	v_lshlrev_b32_e32 v96, 16, v85
	v_and_b32_e32 v97, 0xffff0000, v85
	v_lshlrev_b32_e32 v88, 16, v89
	v_and_b32_e32 v89, 0xffff0000, v89
	v_pk_fma_f32 v[92:93], v[132:133], v[96:97], v[92:93]
	v_lshlrev_b32_e32 v96, 16, v86
	v_pk_mul_f32 v[88:89], v[92:93], v[88:89]
	v_lshlrev_b32_e32 v92, 16, v94
	v_and_b32_e32 v93, 0xffff0000, v94
	v_and_b32_e32 v97, 0xffff0000, v86
	v_cvt_pk_bf16_f32 v85, v88, v89
	v_lshlrev_b32_e32 v88, 16, v90
	v_and_b32_e32 v89, 0xffff0000, v90
	v_pk_fma_f32 v[92:93], v[132:133], v[96:97], v[92:93]
	v_lshlrev_b32_e32 v90, 16, v95
	v_pk_mul_f32 v[88:89], v[92:93], v[88:89]
	v_lshlrev_b32_e32 v92, 16, v87
	v_cvt_pk_bf16_f32 v86, v88, v89
	v_lshlrev_b32_e32 v88, 16, v91
	v_and_b32_e32 v89, 0xffff0000, v91
	v_and_b32_e32 v91, 0xffff0000, v95
	v_and_b32_e32 v93, 0xffff0000, v87
	v_pk_fma_f32 v[90:91], v[132:133], v[92:93], v[90:91]
	s_waitcnt vmcnt(7)
	v_lshlrev_b32_e32 v92, 16, v76
	v_pk_mul_f32 v[88:89], v[90:91], v[88:89]
	v_and_b32_e32 v93, 0xffff0000, v76
	v_cvt_pk_bf16_f32 v87, v88, v89
	global_store_dwordx4 v[104:105], v[84:87], off offset:512
	ds_read_b128 v[84:87], v1 offset:7392
	s_waitcnt vmcnt(7)
	v_lshlrev_b32_e32 v88, 16, v80
	v_and_b32_e32 v89, 0xffff0000, v80
	v_lshlrev_b32_e32 v80, 16, v81
	v_and_b32_e32 v81, 0xffff0000, v81
	s_waitcnt lgkmcnt(0)
	v_lshlrev_b32_e32 v90, 16, v84
	v_and_b32_e32 v91, 0xffff0000, v84
	v_pk_fma_f32 v[90:91], v[132:133], v[92:93], v[90:91]
	v_lshlrev_b32_e32 v84, 16, v85
	v_pk_mul_f32 v[88:89], v[90:91], v[88:89]
	v_and_b32_e32 v85, 0xffff0000, v85
	v_cvt_pk_bf16_f32 v76, v88, v89
	v_lshlrev_b32_e32 v88, 16, v77
	v_and_b32_e32 v89, 0xffff0000, v77
	v_pk_fma_f32 v[84:85], v[132:133], v[88:89], v[84:85]
	v_lshlrev_b32_e32 v88, 16, v78
	v_pk_mul_f32 v[80:81], v[84:85], v[80:81]
	v_lshlrev_b32_e32 v84, 16, v86
	v_and_b32_e32 v85, 0xffff0000, v86
	v_and_b32_e32 v89, 0xffff0000, v78
	v_cvt_pk_bf16_f32 v77, v80, v81
	v_lshlrev_b32_e32 v80, 16, v82
	v_and_b32_e32 v81, 0xffff0000, v82
	v_pk_fma_f32 v[84:85], v[132:133], v[88:89], v[84:85]
	v_lshlrev_b32_e32 v82, 16, v87
	v_pk_mul_f32 v[80:81], v[84:85], v[80:81]
	v_lshlrev_b32_e32 v84, 16, v79
	v_cvt_pk_bf16_f32 v78, v80, v81
	v_lshlrev_b32_e32 v80, 16, v83
	v_and_b32_e32 v81, 0xffff0000, v83
	v_and_b32_e32 v83, 0xffff0000, v87
	v_and_b32_e32 v85, 0xffff0000, v79
	v_pk_fma_f32 v[82:83], v[132:133], v[84:85], v[82:83]
	s_nop 0
	v_pk_mul_f32 v[80:81], v[82:83], v[80:81]
	s_nop 0
	v_cvt_pk_bf16_f32 v79, v80, v81
	global_store_dwordx4 v[102:103], v[76:79], off offset:768
	s_add_u32 s2, s2, 0x8400
	s_addc_u32 s3, s3, 0
	s_cmp_eq_u32 s2, 0x21000
	v_add_u32_e32 v1, 0x2100, v1
	s_cbranch_scc0 .LBB0_822
	s_branch .LBB0_804
